# out-proj GEMM main loop on LDS-DMA staging as well (same generator as in-proj)
# baseline (speedup 1.0000x reference)
;     const int lane = tid & 63, wid = tid >> 6, wr = wid >> 1, wc = wid & 1, fr = lane & 15, fq = lane >> 4;
; #pragma unroll
;     for (int m = 0; m < 4; ++m)
; #pragma unroll
;         for (int n = 0; n < 4; ++n) acc[m][n] = (f32x4){0.f, 0.f, 0.f, 0.f};
;     unsigned ao[4];
; #pragma unroll
;     for (int i = 0; i < 4; ++i) ao[i] = arow((tid >> 3) + 32 * i) + (tid & 7) * 8;
;     const int bk = tid >> 4, bnc = tid & 15;
;     constexpr int NRB = B_F32 ? 8 : 4;
;     u32x4 ra0[4], ra1[4]; u32x4 rb0[NRB], rb1[NRB];
;     auto gloadA = [&](int kt, u32x4 (&ra)[4]) __attribute__((always_inline)) {
; #pragma unroll
;         for (int i = 0; i < 4; ++i) ra[i] = *(const u32x4*)(Abase + (ao[i] + kt * 64));
;     };
;     auto gloadB = [&](int kt, u32x4 (&rb)[NRB]) __attribute__((always_inline)) {
;         if (B_F32) {
;             const float* bp = (const float*)Bbase + (boff + (unsigned)((kt * 64 + bk) * ldb));
; #pragma unroll
;             for (int i = 0; i < 4; ++i) {
;                 if (bval) { rb[2 * i] = *(const u32x4*)(bp + (unsigned)(16 * i * ldb)); rb[2 * i + 1] = *(const u32x4*)(bp + (unsigned)(16 * i * ldb) + 4); }
;                 else { rb[2 * i] = (u32x4){0u, 0u, 0u, 0u}; rb[2 * i + 1] = rb[2 * i]; }
;             }
;         } else {
;             const bf16* bp = (const bf16*)Bbase + (boff + (unsigned)((kt * 64 + bk) * ldb));
; #pragma unroll
;             for (int i = 0; i < 4; ++i) rb[i] = bval ? *(const u32x4*)(bp + (unsigned)(16 * i * ldb)) : (u32x4){0u, 0u, 0u, 0u};
;         }
;     };
;     auto lstore = [&](const u32x4 (&ra)[4], const u32x4 (&rb)[NRB]) __attribute__((always_inline)) {
; #pragma unroll
;         for (int i = 0; i < 4; ++i) { const int row = (tid >> 3) + 32 * i, kc = tid & 7;
; __device__ __forceinline__ void ph_outproj_mfma(const Ctx& c, int layer, int tile, unsigned char* lds) {
;     int mt = tile >> 3; const int nt = tile & 7;
;     if (layer == 1) { if (mt >= 128) return; mt = (mt >> 5) * 34 + 2 + (mt & 31); }
;     const bf16* MIX = c.w<bf16>(WS_MIX) + (size_t)mt * 128 * D;
;     f32x4 acc[4][4];
;     const int bc = nt * 128 + (c.tid & 15) * 8;
;     gemm_tile<false, 1>(c.tid, lds, MIX, [&](int r) __attribute__((always_inline)) { return (unsigned)(r * D); }, c.w<bf16>(WS_BOUT) + (size_t)layer * D * D, (unsigned)bc, D, true, D, acc);
.LBB0_253:
	s_and_b64 vcc, exec, s[6:7]
	s_cbranch_vccz .LBB0_249
	s_waitcnt lgkmcnt(0)
	s_load_dwordx2 s[46:47], s[4:5], 0x130
	s_ashr_i32 s29, s28, 31
	s_and_b32 s6, s15, 0x380
	s_lshl_b64 s[18:19], s[28:29], 18
	v_mov_b32_e32 v12, 0
	s_waitcnt lgkmcnt(0)
	s_add_u32 s7, s46, s18
	s_addc_u32 s17, s47, s19
	s_add_u32 s50, s7, 0xdec6000
	s_addc_u32 s51, s17, 0
	s_lshl_b32 s7, s16, 7
	s_and_b32 s17, s7, 0x380
	s_add_u32 s7, s46, s44
	s_addc_u32 s29, s47, s45
	s_add_u32 s56, s7, 0x18995100
	s_addc_u32 s57, s29, 0
	v_lshl_add_u64 v[6:7], v[134:135], 1, s[50:51]
	v_lshl_add_u64 v[8:9], v[136:137], 1, s[50:51]
	v_or3_b32 v2, s17, v147, v155
	v_lshl_add_u64 v[6:7], v[138:139], 1, s[50:51]
	v_lshl_add_u64 v[8:9], v[2:3], 1, s[56:57]
	v_add_co_u32_e32 v6, vcc, s40, v8
	s_mov_b32 s7, 0x10000
	s_nop 0
	v_addc_co_u32_e32 v7, vcc, 0, v9, vcc
	v_add_co_u32_e32 v10, vcc, s7, v8
	s_mov_b32 s7, 0x18000
	s_nop 0
	v_addc_co_u32_e32 v11, vcc, 0, v9, vcc
	v_lshl_add_u64 v[4:5], v[132:133], 1, s[50:51]
	v_add_co_u32_e32 v6, vcc, s7, v8
	v_addc_co_u32_e32 v7, vcc, 0, v9, vcc
	v_lshl_add_u64 v[4:5], v[140:141], 1, s[50:51]
	v_lshl_add_u64 v[4:5], v[142:143], 1, s[50:51]
	v_lshl_add_u64 v[6:7], v[158:159], 1, s[50:51]
	v_lshl_add_u64 v[4:5], s[46:47], 0, v[164:165]
	v_lshl_add_u64 v[4:5], v[4:5], 0, s[18:19]
	s_mov_b64 s[18:19], 0xdec6180
	v_add_u32_e32 v2, s6, v163
	s_mov_b32 s6, 0
	v_lshl_add_u64 v[116:117], v[4:5], 0, s[18:19]
	v_mov_b32_e32 v118, v161
	s_mov_b64 s[100:101], s[50:51]
	s_mov_b64 s[18:19], s[56:57]
	s_lshl_b32 s98, s17, 1
	v_lshrrev_b32_e32 v215, 6, v156
	v_lshlrev_b32_e32 v215, 5, v215
	v_bfe_u32 v216, v156, 2, 4
	v_add_u32_e32 v215, v215, v216
	v_mul_u32_u24_e32 v215, 0x800, v215
	v_bfe_u32 v216, v156, 4, 2
	v_sub_u32_e32 v216, 0, v216
	v_and_b32_e32 v216, 3, v216
	v_and_b32_e32 v60, 3, v156
	v_xor_b32_e32 v216, v216, v60
	v_lshl_add_u32 v202, v216, 4, v215
	v_add_u32_e32 v203, 64, v202
	v_add_u32_e32 v204, 0x8000, v202
	v_add_u32_e32 v205, 64, v204
	v_lshrrev_b32_e32 v215, 6, v156
	v_lshlrev_b32_e32 v215, 4, v215
	v_bfe_u32 v216, v156, 4, 2
	v_add_u32_e32 v215, v215, v216
	v_mul_u32_u24_e32 v215, 0x800, v215
	v_add_u32_e32 v215, s98, v215
	v_bfe_u32 v60, v156, 1, 3
	v_xor_b32_e32 v60, v60, v216
	v_lshlrev_b32_e32 v60, 1, v60
	v_and_b32_e32 v216, 1, v156
	v_or_b32_e32 v60, v60, v216
	v_lshl_add_u32 v206, v60, 4, v215
	v_add_u32_e32 v207, 0x2000, v206
	v_xor_b32_e32 v60, 8, v60
	v_lshl_add_u32 v208, v60, 4, v215
	v_add_u32_e32 v208, 0x4000, v208
	v_add_u32_e32 v209, 0x2000, v208
	v_bfe_u32 v215, v156, 2, 2
	v_sub_u32_e32 v215, 0, v215
	v_and_b32_e32 v215, 3, v215
	v_lshlrev_b32_e32 v215, 4, v215
	v_xor_b32_e32 v211, v184, v215
	v_bfe_u32 v215, v156, 4, 2
	v_lshlrev_b32_e32 v215, 3, v215
	v_bfe_u32 v216, v156, 2, 2
	v_add_u32_e32 v215, v215, v216
	v_lshlrev_b32_e32 v215, 8, v215
	v_lshrrev_b32_e32 v60, 6, v156
	v_lshrrev_b32_e32 v210, 4, v156
	v_xor_b32_e32 v60, v60, v210
	v_and_b32_e32 v60, 1, v60
	v_lshlrev_b32_e32 v60, 7, v60
	v_or_b32_e32 v215, v215, v60
	v_and_b32_e32 v60, 3, v156
	v_lshlrev_b32_e32 v60, 3, v60
	v_or_b32_e32 v215, v215, v60
	v_xor_b32_e32 v60, 0, v216
	v_lshl_or_b32 v210, v60, 5, v215
	v_xor_b32_e32 v60, 1, v216
	v_lshl_or_b32 v212, v60, 5, v215
	v_xor_b32_e32 v60, 2, v216
	v_lshl_or_b32 v213, v60, 5, v215
	v_xor_b32_e32 v60, 3, v216
	v_lshl_or_b32 v214, v60, 5, v215
	v_lshrrev_b32_e32 v215, 6, v156
	s_nop 1
	v_readfirstlane_b32 s98, v215
	s_nop 1
	s_lshl_b32 s99, s98, 12
	s_lshl_b32 s98, s98, 11
	s_barrier
	s_add_u32 m0, s98, 0x0
	s_nop 0
	global_load_lds_dwordx4 v202, s[100:101]
	s_add_u32 m0, s98, 0x2040
	s_nop 0
	global_load_lds_dwordx4 v203, s[100:101]
	s_add_u32 m0, s98, 0x400
	s_nop 0
	global_load_lds_dwordx4 v204, s[100:101]
	s_add_u32 m0, s98, 0x2440
	s_nop 0
	global_load_lds_dwordx4 v205, s[100:101]
	s_add_u32 m0, s99, 0x4080
	s_nop 0
	global_load_lds_dwordx4 v206, s[18:19]
	s_add_u32 m0, s99, 0x4480
	s_nop 0
	global_load_lds_dwordx4 v207, s[18:19]
	s_add_u32 m0, s99, 0x4880
	s_nop 0
	global_load_lds_dwordx4 v208, s[18:19]
	s_add_u32 m0, s99, 0x4c80
	s_nop 0
	global_load_lds_dwordx4 v209, s[18:19]
	s_add_u32 s100, s100, 0x80
	s_addc_u32 s101, s101, 0
	s_add_u32 s18, s18, 0x20000
	s_addc_u32 s19, s19, 0
	s_mov_b32 s6, 0
	v_mov_b32_e32 v13, v12
	v_mov_b32_e32 v14, v12
	v_mov_b32_e32 v15, v12
	v_mov_b32_e32 v20, v12
	v_mov_b32_e32 v21, v12
	v_mov_b32_e32 v22, v12
	v_mov_b32_e32 v23, v12
	v_mov_b32_e32 v4, v12
	v_mov_b32_e32 v5, v12
	v_mov_b32_e32 v6, v12
	v_mov_b32_e32 v7, v12
	v_mov_b32_e32 v8, v12
	v_mov_b32_e32 v9, v12
	v_mov_b32_e32 v10, v12
	v_mov_b32_e32 v11, v12
	v_mov_b32_e32 v16, v12
	v_mov_b32_e32 v17, v12
	v_mov_b32_e32 v18, v12
	v_mov_b32_e32 v19, v12
	v_mov_b32_e32 v24, v12
	v_mov_b32_e32 v25, v12
	v_mov_b32_e32 v26, v12
	v_mov_b32_e32 v27, v12
	v_mov_b32_e32 v28, v12
	v_mov_b32_e32 v29, v12
	v_mov_b32_e32 v30, v12
	v_mov_b32_e32 v31, v12
	v_mov_b32_e32 v32, v12
	v_mov_b32_e32 v33, v12
	v_mov_b32_e32 v34, v12
	v_mov_b32_e32 v35, v12
	v_mov_b32_e32 v36, v12
	v_mov_b32_e32 v37, v12
	v_mov_b32_e32 v38, v12
	v_mov_b32_e32 v39, v12
	v_mov_b32_e32 v40, v12
	v_mov_b32_e32 v41, v12
	v_mov_b32_e32 v42, v12
	v_mov_b32_e32 v43, v12
	v_mov_b32_e32 v44, v12
	v_mov_b32_e32 v45, v12
	v_mov_b32_e32 v46, v12
	v_mov_b32_e32 v47, v12
	v_mov_b32_e32 v48, v12
	v_mov_b32_e32 v49, v12
	v_mov_b32_e32 v50, v12
	v_mov_b32_e32 v51, v12
	v_mov_b32_e32 v52, v12
	v_mov_b32_e32 v53, v12
	v_mov_b32_e32 v54, v12
	v_mov_b32_e32 v55, v12
	v_mov_b32_e32 v56, v12
	v_mov_b32_e32 v57, v12
	v_mov_b32_e32 v58, v12
	v_mov_b32_e32 v59, v12
	v_mov_b32_e32 v64, v12
	v_mov_b32_e32 v65, v12
	v_mov_b32_e32 v66, v12
	v_mov_b32_e32 v67, v12
	v_mov_b32_e32 v72, v12
	v_mov_b32_e32 v73, v12
	v_mov_b32_e32 v74, v12
	v_mov_b32_e32 v75, v12
	s_waitcnt vmcnt(0)
	s_barrier
; #define LAS __attribute__((address_space(3)))
; __device__ __forceinline__ s16x4 lds_tr(lds_cptr p) { return __builtin_bit_cast(s16x4, __builtin_amdgcn_ds_read_tr16_b64_v4i16((LAS s16x4*)p)); }
;     ...
;     auto compute = [&]() __attribute__((always_inline)) {
; #pragma unroll
;         for (int kh = 0; kh < 2; ++kh) {
;             bf16x8 af[4], bfr[4];
; #pragma unroll
;             for (int m = 0; m < 4; ++m) af[m] = *(const LAS bf16x8*)(la + kh * GA_KH + m * 1024);
; #pragma unroll
;             for (int n = 0; n < 4; ++n) {
;                 const s16x4 r0 = lds_tr(lb + kh * 32 * GB_ST + n * 32), r1 = lds_tr(lb + kh * 32 * GB_ST + n * 32 + bsw);
;                 bfr[n] = (bf16x8){r0[0], r0[1], r0[2], r0[3], r1[0], r1[1], r1[2], r1[3]};
;             }
; #pragma unroll
;             for (int m = 0; m < 4; ++m)
; #pragma unroll
;                 for (int n = 0; n < 4; ++n) acc[m][n] = __builtin_amdgcn_mfma_f32_16x16x32_bf16(bfr[n], af[m], acc[m][n], 0, 0, 0);
;         }
;     };
;     ...
;     if (DEEP == 1) {
;         gloadA(0, ra0); gloadB(0, rb0); gloadA(1, ra1);
;         for (int kt = 0; kt < nk; kt += 2) {
;             __syncthreads();
;             lstore(ra0, rb0);
;             __syncthreads();
;             gloadB(kt + 1, rb0);
;             if (kt + 2 < nk) gloadA(kt + 2, ra0);
;             compute();
.Lop_loop:
	s_add_u32 m0, s98, 0x9000
	ds_read_b64_tr_b16 v[166:167], v210 offset:16512
	ds_read_b64_tr_b16 v[168:169], v210 offset:17536
	ds_read_b128 v[116:119], v211
	ds_read_b64_tr_b16 v[170:171], v212 offset:16512
	ds_read_b64_tr_b16 v[172:173], v212 offset:17536
	s_waitcnt lgkmcnt(2)
	v_mfma_f32_16x16x32_bf16 v[72:75], v[166:169], v[116:119], v[72:75]
	global_load_lds_dwordx4 v202, s[100:101]
	s_add_u32 m0, s98, 0xb040
	ds_read_b64_tr_b16 v[174:175], v213 offset:16512
	ds_read_b64_tr_b16 v[176:177], v213 offset:17536
	s_waitcnt lgkmcnt(2)
	v_mfma_f32_16x16x32_bf16 v[64:67], v[170:173], v[116:119], v[64:67]
	global_load_lds_dwordx4 v203, s[100:101]
	s_add_u32 m0, s98, 0x9400
	ds_read_b64_tr_b16 v[178:179], v214 offset:16512
	ds_read_b64_tr_b16 v[180:181], v214 offset:17536
	s_waitcnt lgkmcnt(2)
	v_mfma_f32_16x16x32_bf16 v[56:59], v[174:177], v[116:119], v[56:59]
	global_load_lds_dwordx4 v204, s[100:101]
	s_add_u32 m0, s98, 0xb440
	ds_read_b128 v[120:123], v211 offset:1024
	s_waitcnt lgkmcnt(1)
	v_mfma_f32_16x16x32_bf16 v[52:55], v[178:181], v[116:119], v[52:55]
	global_load_lds_dwordx4 v205, s[100:101]
	s_add_u32 m0, s99, 0xd080
	ds_read_b128 v[124:127], v211 offset:2048
	s_waitcnt lgkmcnt(1)
	v_mfma_f32_16x16x32_bf16 v[48:51], v[166:169], v[120:123], v[48:51]
	global_load_lds_dwordx4 v206, s[18:19]
	s_add_u32 m0, s99, 0xd480
	ds_read_b128 v[128:131], v211 offset:3072
	v_mfma_f32_16x16x32_bf16 v[44:47], v[170:173], v[120:123], v[44:47]
	global_load_lds_dwordx4 v207, s[18:19]
	s_add_u32 m0, s99, 0xd880
	ds_read_b64_tr_b16 v[186:187], v210 offset:24704
	ds_read_b64_tr_b16 v[188:189], v210 offset:25728
	v_mfma_f32_16x16x32_bf16 v[40:43], v[174:177], v[120:123], v[40:43]
	global_load_lds_dwordx4 v208, s[18:19]
	s_add_u32 m0, s99, 0xdc80
	ds_read_b64_tr_b16 v[190:191], v212 offset:24704
	ds_read_b64_tr_b16 v[192:193], v212 offset:25728
	v_mfma_f32_16x16x32_bf16 v[36:39], v[178:181], v[120:123], v[36:39]
	global_load_lds_dwordx4 v209, s[18:19]
	s_add_u32 s100, s100, 0x80
	s_addc_u32 s101, s101, 0
	s_add_u32 s18, s18, 0x20000
	s_addc_u32 s19, s19, 0
	ds_read_b128 v[116:119], v211 offset:8256
	s_waitcnt lgkmcnt(6)
	v_mfma_f32_16x16x32_bf16 v[32:35], v[166:169], v[124:127], v[32:35]
	ds_read_b64_tr_b16 v[194:195], v213 offset:24704
	ds_read_b64_tr_b16 v[196:197], v213 offset:25728
	v_mfma_f32_16x16x32_bf16 v[28:31], v[170:173], v[124:127], v[28:31]
	ds_read_b64_tr_b16 v[198:199], v214 offset:24704
	ds_read_b64_tr_b16 v[200:201], v214 offset:25728
	v_mfma_f32_16x16x32_bf16 v[24:27], v[174:177], v[124:127], v[24:27]
	v_mfma_f32_16x16x32_bf16 v[16:19], v[178:181], v[124:127], v[16:19]
	ds_read_b128 v[120:123], v211 offset:9280
	s_waitcnt lgkmcnt(10)
	v_mfma_f32_16x16x32_bf16 v[8:11], v[166:169], v[128:131], v[8:11]
	v_mfma_f32_16x16x32_bf16 v[4:7], v[170:173], v[128:131], v[4:7]
	v_mfma_f32_16x16x32_bf16 v[20:23], v[174:177], v[128:131], v[20:23]
	v_mfma_f32_16x16x32_bf16 v[12:15], v[178:181], v[128:131], v[12:15]
	ds_read_b128 v[124:127], v211 offset:10304
	s_waitcnt lgkmcnt(6)
	v_mfma_f32_16x16x32_bf16 v[72:75], v[186:189], v[116:119], v[72:75]
	v_mfma_f32_16x16x32_bf16 v[64:67], v[190:193], v[116:119], v[64:67]
	s_waitcnt lgkmcnt(4)
	v_mfma_f32_16x16x32_bf16 v[56:59], v[194:197], v[116:119], v[56:59]
	s_waitcnt lgkmcnt(2)
	v_mfma_f32_16x16x32_bf16 v[52:55], v[198:201], v[116:119], v[52:55]
	ds_read_b128 v[128:131], v211 offset:11328
	s_waitcnt lgkmcnt(2)
	v_mfma_f32_16x16x32_bf16 v[48:51], v[186:189], v[120:123], v[48:51]
	v_mfma_f32_16x16x32_bf16 v[44:47], v[190:193], v[120:123], v[44:47]
	v_mfma_f32_16x16x32_bf16 v[40:43], v[194:197], v[120:123], v[40:43]
	v_mfma_f32_16x16x32_bf16 v[36:39], v[198:201], v[120:123], v[36:39]
	s_waitcnt lgkmcnt(1)
	v_mfma_f32_16x16x32_bf16 v[32:35], v[186:189], v[124:127], v[32:35]
	v_mfma_f32_16x16x32_bf16 v[28:31], v[190:193], v[124:127], v[28:31]
	v_mfma_f32_16x16x32_bf16 v[24:27], v[194:197], v[124:127], v[24:27]
	v_mfma_f32_16x16x32_bf16 v[16:19], v[198:201], v[124:127], v[16:19]
	s_waitcnt lgkmcnt(0)
	v_mfma_f32_16x16x32_bf16 v[8:11], v[186:189], v[128:131], v[8:11]
	v_mfma_f32_16x16x32_bf16 v[4:7], v[190:193], v[128:131], v[4:7]
	v_mfma_f32_16x16x32_bf16 v[20:23], v[194:197], v[128:131], v[20:23]
	v_mfma_f32_16x16x32_bf16 v[12:15], v[198:201], v[128:131], v[12:15]
	s_waitcnt vmcnt(0) lgkmcnt(0)
	s_barrier
; #define LAS __attribute__((address_space(3)))
; __device__ __forceinline__ s16x4 lds_tr(lds_cptr p) { return __builtin_bit_cast(s16x4, __builtin_amdgcn_ds_read_tr16_b64_v4i16((LAS s16x4*)p)); }
;     ...
;     auto compute = [&]() __attribute__((always_inline)) {
; #pragma unroll
;         for (int kh = 0; kh < 2; ++kh) {
;             bf16x8 af[4], bfr[4];
; #pragma unroll
;             for (int m = 0; m < 4; ++m) af[m] = *(const LAS bf16x8*)(la + kh * GA_KH + m * 1024);
; #pragma unroll
;             for (int n = 0; n < 4; ++n) {
;                 const s16x4 r0 = lds_tr(lb + kh * 32 * GB_ST + n * 32), r1 = lds_tr(lb + kh * 32 * GB_ST + n * 32 + bsw);
;                 bfr[n] = (bf16x8){r0[0], r0[1], r0[2], r0[3], r1[0], r1[1], r1[2], r1[3]};
;             }
; #pragma unroll
;             for (int m = 0; m < 4; ++m)
; #pragma unroll
;                 for (int n = 0; n < 4; ++n) acc[m][n] = __builtin_amdgcn_mfma_f32_16x16x32_bf16(bfr[n], af[m], acc[m][n], 0, 0, 0);
;         }
;     };
;     ...
;             __syncthreads();
;             lstore(ra1, rb0);
;             __syncthreads();
;             if (kt + 2 < nk) gloadB(kt + 2, rb0);
;             if (kt + 3 < nk) gloadA(kt + 3, ra1);
;             compute();
;         }
;         return;
;     }
	s_add_u32 m0, s98, 0x0
	ds_read_b64_tr_b16 v[166:167], v210 offset:53376
	ds_read_b64_tr_b16 v[168:169], v210 offset:54400
	ds_read_b128 v[116:119], v211 offset:36864
	ds_read_b64_tr_b16 v[170:171], v212 offset:53376
	ds_read_b64_tr_b16 v[172:173], v212 offset:54400
	s_waitcnt lgkmcnt(2)
	v_mfma_f32_16x16x32_bf16 v[72:75], v[166:169], v[116:119], v[72:75]
	global_load_lds_dwordx4 v202, s[100:101]
	s_add_u32 m0, s98, 0x2040
	ds_read_b64_tr_b16 v[174:175], v213 offset:53376
	ds_read_b64_tr_b16 v[176:177], v213 offset:54400
	s_waitcnt lgkmcnt(2)
	v_mfma_f32_16x16x32_bf16 v[64:67], v[170:173], v[116:119], v[64:67]
	global_load_lds_dwordx4 v203, s[100:101]
	s_add_u32 m0, s98, 0x400
	ds_read_b64_tr_b16 v[178:179], v214 offset:53376
	ds_read_b64_tr_b16 v[180:181], v214 offset:54400
	s_waitcnt lgkmcnt(2)
	v_mfma_f32_16x16x32_bf16 v[56:59], v[174:177], v[116:119], v[56:59]
	global_load_lds_dwordx4 v204, s[100:101]
	s_add_u32 m0, s98, 0x2440
	ds_read_b128 v[120:123], v211 offset:37888
	s_waitcnt lgkmcnt(1)
	v_mfma_f32_16x16x32_bf16 v[52:55], v[178:181], v[116:119], v[52:55]
	global_load_lds_dwordx4 v205, s[100:101]
	s_add_u32 m0, s99, 0x4080
	ds_read_b128 v[124:127], v211 offset:38912
	s_waitcnt lgkmcnt(1)
	v_mfma_f32_16x16x32_bf16 v[48:51], v[166:169], v[120:123], v[48:51]
	global_load_lds_dwordx4 v206, s[18:19]
	s_add_u32 m0, s99, 0x4480
	ds_read_b128 v[128:131], v211 offset:39936
	v_mfma_f32_16x16x32_bf16 v[44:47], v[170:173], v[120:123], v[44:47]
	global_load_lds_dwordx4 v207, s[18:19]
	s_add_u32 m0, s99, 0x4880
	ds_read_b64_tr_b16 v[186:187], v210 offset:61568
	ds_read_b64_tr_b16 v[188:189], v210 offset:62592
	v_mfma_f32_16x16x32_bf16 v[40:43], v[174:177], v[120:123], v[40:43]
	global_load_lds_dwordx4 v208, s[18:19]
	s_add_u32 m0, s99, 0x4c80
	ds_read_b64_tr_b16 v[190:191], v212 offset:61568
	ds_read_b64_tr_b16 v[192:193], v212 offset:62592
	v_mfma_f32_16x16x32_bf16 v[36:39], v[178:181], v[120:123], v[36:39]
	global_load_lds_dwordx4 v209, s[18:19]
	s_add_u32 s100, s100, 0x80
	s_addc_u32 s101, s101, 0
	s_add_u32 s18, s18, 0x20000
	s_addc_u32 s19, s19, 0
	ds_read_b128 v[116:119], v211 offset:45120
	s_waitcnt lgkmcnt(6)
	v_mfma_f32_16x16x32_bf16 v[32:35], v[166:169], v[124:127], v[32:35]
	ds_read_b64_tr_b16 v[194:195], v213 offset:61568
	ds_read_b64_tr_b16 v[196:197], v213 offset:62592
	v_mfma_f32_16x16x32_bf16 v[28:31], v[170:173], v[124:127], v[28:31]
	ds_read_b64_tr_b16 v[198:199], v214 offset:61568
	ds_read_b64_tr_b16 v[200:201], v214 offset:62592
	v_mfma_f32_16x16x32_bf16 v[24:27], v[174:177], v[124:127], v[24:27]
	v_mfma_f32_16x16x32_bf16 v[16:19], v[178:181], v[124:127], v[16:19]
	ds_read_b128 v[120:123], v211 offset:46144
	s_waitcnt lgkmcnt(10)
	v_mfma_f32_16x16x32_bf16 v[8:11], v[166:169], v[128:131], v[8:11]
	v_mfma_f32_16x16x32_bf16 v[4:7], v[170:173], v[128:131], v[4:7]
	v_mfma_f32_16x16x32_bf16 v[20:23], v[174:177], v[128:131], v[20:23]
	v_mfma_f32_16x16x32_bf16 v[12:15], v[178:181], v[128:131], v[12:15]
	ds_read_b128 v[124:127], v211 offset:47168
	s_waitcnt lgkmcnt(6)
	v_mfma_f32_16x16x32_bf16 v[72:75], v[186:189], v[116:119], v[72:75]
	v_mfma_f32_16x16x32_bf16 v[64:67], v[190:193], v[116:119], v[64:67]
	s_waitcnt lgkmcnt(4)
	v_mfma_f32_16x16x32_bf16 v[56:59], v[194:197], v[116:119], v[56:59]
	s_waitcnt lgkmcnt(2)
	v_mfma_f32_16x16x32_bf16 v[52:55], v[198:201], v[116:119], v[52:55]
	ds_read_b128 v[128:131], v211 offset:48192
	s_waitcnt lgkmcnt(2)
	v_mfma_f32_16x16x32_bf16 v[48:51], v[186:189], v[120:123], v[48:51]
	v_mfma_f32_16x16x32_bf16 v[44:47], v[190:193], v[120:123], v[44:47]
	v_mfma_f32_16x16x32_bf16 v[40:43], v[194:197], v[120:123], v[40:43]
	v_mfma_f32_16x16x32_bf16 v[36:39], v[198:201], v[120:123], v[36:39]
	s_waitcnt lgkmcnt(1)
	v_mfma_f32_16x16x32_bf16 v[32:35], v[186:189], v[124:127], v[32:35]
	v_mfma_f32_16x16x32_bf16 v[28:31], v[190:193], v[124:127], v[28:31]
	v_mfma_f32_16x16x32_bf16 v[24:27], v[194:197], v[124:127], v[24:27]
	v_mfma_f32_16x16x32_bf16 v[16:19], v[198:201], v[124:127], v[16:19]
	s_waitcnt lgkmcnt(0)
	v_mfma_f32_16x16x32_bf16 v[8:11], v[186:189], v[128:131], v[8:11]
	v_mfma_f32_16x16x32_bf16 v[4:7], v[190:193], v[128:131], v[4:7]
	v_mfma_f32_16x16x32_bf16 v[20:23], v[194:197], v[128:131], v[20:23]
	v_mfma_f32_16x16x32_bf16 v[12:15], v[198:201], v[128:131], v[12:15]
	s_waitcnt vmcnt(0) lgkmcnt(0)
	s_barrier
	s_add_i32 s6, s6, 2
	s_cmp_lt_u32 s6, 14
	s_cbranch_scc1 .Lop_loop
; #define LAS __attribute__((address_space(3)))
; __device__ __forceinline__ s16x4 lds_tr(lds_cptr p) { return __builtin_bit_cast(s16x4, __builtin_amdgcn_ds_read_tr16_b64_v4i16((LAS s16x4*)p)); }
;     ...
;     auto compute = [&]() __attribute__((always_inline)) {
; #pragma unroll
;         for (int kh = 0; kh < 2; ++kh) {
;             bf16x8 af[4], bfr[4];
; #pragma unroll
;             for (int m = 0; m < 4; ++m) af[m] = *(const LAS bf16x8*)(la + kh * GA_KH + m * 1024);
; #pragma unroll
;             for (int n = 0; n < 4; ++n) {
;                 const s16x4 r0 = lds_tr(lb + kh * 32 * GB_ST + n * 32), r1 = lds_tr(lb + kh * 32 * GB_ST + n * 32 + bsw);
;                 bfr[n] = (bf16x8){r0[0], r0[1], r0[2], r0[3], r1[0], r1[1], r1[2], r1[3]};
;             }
; #pragma unroll
;             for (int m = 0; m < 4; ++m)
; #pragma unroll
;                 for (int n = 0; n < 4; ++n) acc[m][n] = __builtin_amdgcn_mfma_f32_16x16x32_bf16(bfr[n], af[m], acc[m][n], 0, 0, 0);
;         }
;     };
;     ...
;     if (DEEP == 1) {
;         gloadA(0, ra0); gloadB(0, rb0); gloadA(1, ra1);
;         for (int kt = 0; kt < nk; kt += 2) {
;             __syncthreads();
;             lstore(ra0, rb0);
;             __syncthreads();
;             gloadB(kt + 1, rb0);
;             if (kt + 2 < nk) gloadA(kt + 2, ra0);
;             compute();
	s_add_u32 m0, s98, 0x9000
	ds_read_b64_tr_b16 v[166:167], v210 offset:16512
	ds_read_b64_tr_b16 v[168:169], v210 offset:17536
	ds_read_b128 v[116:119], v211
	ds_read_b64_tr_b16 v[170:171], v212 offset:16512
	ds_read_b64_tr_b16 v[172:173], v212 offset:17536
	s_waitcnt lgkmcnt(2)
	v_mfma_f32_16x16x32_bf16 v[72:75], v[166:169], v[116:119], v[72:75]
	global_load_lds_dwordx4 v202, s[100:101]
	s_add_u32 m0, s98, 0xb040
	ds_read_b64_tr_b16 v[174:175], v213 offset:16512
	ds_read_b64_tr_b16 v[176:177], v213 offset:17536
	s_waitcnt lgkmcnt(2)
	v_mfma_f32_16x16x32_bf16 v[64:67], v[170:173], v[116:119], v[64:67]
	global_load_lds_dwordx4 v203, s[100:101]
	s_add_u32 m0, s98, 0x9400
	ds_read_b64_tr_b16 v[178:179], v214 offset:16512
	ds_read_b64_tr_b16 v[180:181], v214 offset:17536
	s_waitcnt lgkmcnt(2)
	v_mfma_f32_16x16x32_bf16 v[56:59], v[174:177], v[116:119], v[56:59]
	global_load_lds_dwordx4 v204, s[100:101]
	s_add_u32 m0, s98, 0xb440
	ds_read_b128 v[120:123], v211 offset:1024
	s_waitcnt lgkmcnt(1)
	v_mfma_f32_16x16x32_bf16 v[52:55], v[178:181], v[116:119], v[52:55]
	global_load_lds_dwordx4 v205, s[100:101]
	s_add_u32 m0, s99, 0xd080
	ds_read_b128 v[124:127], v211 offset:2048
	s_waitcnt lgkmcnt(1)
	v_mfma_f32_16x16x32_bf16 v[48:51], v[166:169], v[120:123], v[48:51]
	global_load_lds_dwordx4 v206, s[18:19]
	s_add_u32 m0, s99, 0xd480
	ds_read_b128 v[128:131], v211 offset:3072
	v_mfma_f32_16x16x32_bf16 v[44:47], v[170:173], v[120:123], v[44:47]
	global_load_lds_dwordx4 v207, s[18:19]
	s_add_u32 m0, s99, 0xd880
	ds_read_b64_tr_b16 v[186:187], v210 offset:24704
	ds_read_b64_tr_b16 v[188:189], v210 offset:25728
	v_mfma_f32_16x16x32_bf16 v[40:43], v[174:177], v[120:123], v[40:43]
	global_load_lds_dwordx4 v208, s[18:19]
	s_add_u32 m0, s99, 0xdc80
	ds_read_b64_tr_b16 v[190:191], v212 offset:24704
	ds_read_b64_tr_b16 v[192:193], v212 offset:25728
	v_mfma_f32_16x16x32_bf16 v[36:39], v[178:181], v[120:123], v[36:39]
	global_load_lds_dwordx4 v209, s[18:19]
	s_add_u32 s100, s100, 0x80
	s_addc_u32 s101, s101, 0
	s_add_u32 s18, s18, 0x20000
	s_addc_u32 s19, s19, 0
	ds_read_b128 v[116:119], v211 offset:8256
	s_waitcnt lgkmcnt(6)
	v_mfma_f32_16x16x32_bf16 v[32:35], v[166:169], v[124:127], v[32:35]
	ds_read_b64_tr_b16 v[194:195], v213 offset:24704
	ds_read_b64_tr_b16 v[196:197], v213 offset:25728
	v_mfma_f32_16x16x32_bf16 v[28:31], v[170:173], v[124:127], v[28:31]
	ds_read_b64_tr_b16 v[198:199], v214 offset:24704
	ds_read_b64_tr_b16 v[200:201], v214 offset:25728
	v_mfma_f32_16x16x32_bf16 v[24:27], v[174:177], v[124:127], v[24:27]
	v_mfma_f32_16x16x32_bf16 v[16:19], v[178:181], v[124:127], v[16:19]
	ds_read_b128 v[120:123], v211 offset:9280
	s_waitcnt lgkmcnt(10)
	v_mfma_f32_16x16x32_bf16 v[8:11], v[166:169], v[128:131], v[8:11]
	v_mfma_f32_16x16x32_bf16 v[4:7], v[170:173], v[128:131], v[4:7]
	v_mfma_f32_16x16x32_bf16 v[20:23], v[174:177], v[128:131], v[20:23]
	v_mfma_f32_16x16x32_bf16 v[12:15], v[178:181], v[128:131], v[12:15]
	ds_read_b128 v[124:127], v211 offset:10304
	s_waitcnt lgkmcnt(6)
	v_mfma_f32_16x16x32_bf16 v[72:75], v[186:189], v[116:119], v[72:75]
	v_mfma_f32_16x16x32_bf16 v[64:67], v[190:193], v[116:119], v[64:67]
	s_waitcnt lgkmcnt(4)
	v_mfma_f32_16x16x32_bf16 v[56:59], v[194:197], v[116:119], v[56:59]
	s_waitcnt lgkmcnt(2)
	v_mfma_f32_16x16x32_bf16 v[52:55], v[198:201], v[116:119], v[52:55]
	ds_read_b128 v[128:131], v211 offset:11328
	s_waitcnt lgkmcnt(2)
	v_mfma_f32_16x16x32_bf16 v[48:51], v[186:189], v[120:123], v[48:51]
	v_mfma_f32_16x16x32_bf16 v[44:47], v[190:193], v[120:123], v[44:47]
	v_mfma_f32_16x16x32_bf16 v[40:43], v[194:197], v[120:123], v[40:43]
	v_mfma_f32_16x16x32_bf16 v[36:39], v[198:201], v[120:123], v[36:39]
	s_waitcnt lgkmcnt(1)
	v_mfma_f32_16x16x32_bf16 v[32:35], v[186:189], v[124:127], v[32:35]
	v_mfma_f32_16x16x32_bf16 v[28:31], v[190:193], v[124:127], v[28:31]
	v_mfma_f32_16x16x32_bf16 v[24:27], v[194:197], v[124:127], v[24:27]
	v_mfma_f32_16x16x32_bf16 v[16:19], v[198:201], v[124:127], v[16:19]
	s_waitcnt lgkmcnt(0)
	v_mfma_f32_16x16x32_bf16 v[8:11], v[186:189], v[128:131], v[8:11]
	v_mfma_f32_16x16x32_bf16 v[4:7], v[190:193], v[128:131], v[4:7]
	v_mfma_f32_16x16x32_bf16 v[20:23], v[194:197], v[128:131], v[20:23]
	v_mfma_f32_16x16x32_bf16 v[12:15], v[198:201], v[128:131], v[12:15]
	s_waitcnt vmcnt(0) lgkmcnt(0)
	s_barrier
; #define LAS __attribute__((address_space(3)))
; __device__ __forceinline__ s16x4 lds_tr(lds_cptr p) { return __builtin_bit_cast(s16x4, __builtin_amdgcn_ds_read_tr16_b64_v4i16((LAS s16x4*)p)); }
;     ...
;     auto compute = [&]() __attribute__((always_inline)) {
; #pragma unroll
;         for (int kh = 0; kh < 2; ++kh) {
;             bf16x8 af[4], bfr[4];
; #pragma unroll
;             for (int m = 0; m < 4; ++m) af[m] = *(const LAS bf16x8*)(la + kh * GA_KH + m * 1024);
; #pragma unroll
;             for (int n = 0; n < 4; ++n) {
;                 const s16x4 r0 = lds_tr(lb + kh * 32 * GB_ST + n * 32), r1 = lds_tr(lb + kh * 32 * GB_ST + n * 32 + bsw);
;                 bfr[n] = (bf16x8){r0[0], r0[1], r0[2], r0[3], r1[0], r1[1], r1[2], r1[3]};
;             }
; #pragma unroll
;             for (int m = 0; m < 4; ++m)
; #pragma unroll
;                 for (int n = 0; n < 4; ++n) acc[m][n] = __builtin_amdgcn_mfma_f32_16x16x32_bf16(bfr[n], af[m], acc[m][n], 0, 0, 0);
;         }
;     };
	ds_read_b64_tr_b16 v[166:167], v210 offset:53376
	ds_read_b64_tr_b16 v[168:169], v210 offset:54400
	ds_read_b128 v[116:119], v211 offset:36864
	ds_read_b64_tr_b16 v[170:171], v212 offset:53376
	ds_read_b64_tr_b16 v[172:173], v212 offset:54400
	s_waitcnt lgkmcnt(2)
	v_mfma_f32_16x16x32_bf16 v[72:75], v[166:169], v[116:119], v[72:75]
	ds_read_b64_tr_b16 v[174:175], v213 offset:53376
	ds_read_b64_tr_b16 v[176:177], v213 offset:54400
	s_waitcnt lgkmcnt(2)
	v_mfma_f32_16x16x32_bf16 v[64:67], v[170:173], v[116:119], v[64:67]
	ds_read_b64_tr_b16 v[178:179], v214 offset:53376
	ds_read_b64_tr_b16 v[180:181], v214 offset:54400
	s_waitcnt lgkmcnt(2)
	v_mfma_f32_16x16x32_bf16 v[56:59], v[174:177], v[116:119], v[56:59]
	ds_read_b128 v[120:123], v211 offset:37888
	s_waitcnt lgkmcnt(1)
	v_mfma_f32_16x16x32_bf16 v[52:55], v[178:181], v[116:119], v[52:55]
	ds_read_b128 v[124:127], v211 offset:38912
	s_waitcnt lgkmcnt(1)
	v_mfma_f32_16x16x32_bf16 v[48:51], v[166:169], v[120:123], v[48:51]
	ds_read_b128 v[128:131], v211 offset:39936
	v_mfma_f32_16x16x32_bf16 v[44:47], v[170:173], v[120:123], v[44:47]
	ds_read_b64_tr_b16 v[186:187], v210 offset:61568
	ds_read_b64_tr_b16 v[188:189], v210 offset:62592
	v_mfma_f32_16x16x32_bf16 v[40:43], v[174:177], v[120:123], v[40:43]
	ds_read_b64_tr_b16 v[190:191], v212 offset:61568
	ds_read_b64_tr_b16 v[192:193], v212 offset:62592
	v_mfma_f32_16x16x32_bf16 v[36:39], v[178:181], v[120:123], v[36:39]
	ds_read_b128 v[116:119], v211 offset:45120
	s_waitcnt lgkmcnt(6)
	v_mfma_f32_16x16x32_bf16 v[32:35], v[166:169], v[124:127], v[32:35]
	ds_read_b64_tr_b16 v[194:195], v213 offset:61568
	ds_read_b64_tr_b16 v[196:197], v213 offset:62592
	v_mfma_f32_16x16x32_bf16 v[28:31], v[170:173], v[124:127], v[28:31]
	ds_read_b64_tr_b16 v[198:199], v214 offset:61568
	ds_read_b64_tr_b16 v[200:201], v214 offset:62592
	v_mfma_f32_16x16x32_bf16 v[24:27], v[174:177], v[124:127], v[24:27]
	v_mfma_f32_16x16x32_bf16 v[16:19], v[178:181], v[124:127], v[16:19]
	ds_read_b128 v[120:123], v211 offset:46144
	s_waitcnt lgkmcnt(10)
	v_mfma_f32_16x16x32_bf16 v[8:11], v[166:169], v[128:131], v[8:11]
	v_mfma_f32_16x16x32_bf16 v[4:7], v[170:173], v[128:131], v[4:7]
	v_mfma_f32_16x16x32_bf16 v[20:23], v[174:177], v[128:131], v[20:23]
	v_mfma_f32_16x16x32_bf16 v[12:15], v[178:181], v[128:131], v[12:15]
	ds_read_b128 v[124:127], v211 offset:47168
	s_waitcnt lgkmcnt(6)
	v_mfma_f32_16x16x32_bf16 v[72:75], v[186:189], v[116:119], v[72:75]
	v_mfma_f32_16x16x32_bf16 v[64:67], v[190:193], v[116:119], v[64:67]
	s_waitcnt lgkmcnt(4)
	v_mfma_f32_16x16x32_bf16 v[56:59], v[194:197], v[116:119], v[56:59]
	s_waitcnt lgkmcnt(2)
	v_mfma_f32_16x16x32_bf16 v[52:55], v[198:201], v[116:119], v[52:55]
	ds_read_b128 v[128:131], v211 offset:48192
	s_waitcnt lgkmcnt(2)
	v_mfma_f32_16x16x32_bf16 v[48:51], v[186:189], v[120:123], v[48:51]
	v_mfma_f32_16x16x32_bf16 v[44:47], v[190:193], v[120:123], v[44:47]
	v_mfma_f32_16x16x32_bf16 v[40:43], v[194:197], v[120:123], v[40:43]
	v_mfma_f32_16x16x32_bf16 v[36:39], v[198:201], v[120:123], v[36:39]
	s_waitcnt lgkmcnt(1)
	v_mfma_f32_16x16x32_bf16 v[32:35], v[186:189], v[124:127], v[32:35]
	v_mfma_f32_16x16x32_bf16 v[28:31], v[190:193], v[124:127], v[28:31]
	v_mfma_f32_16x16x32_bf16 v[24:27], v[194:197], v[124:127], v[24:27]
	v_mfma_f32_16x16x32_bf16 v[16:19], v[198:201], v[124:127], v[16:19]
	s_waitcnt lgkmcnt(0)
	v_mfma_f32_16x16x32_bf16 v[8:11], v[186:189], v[128:131], v[8:11]
	v_mfma_f32_16x16x32_bf16 v[4:7], v[190:193], v[128:131], v[4:7]
	v_mfma_f32_16x16x32_bf16 v[20:23], v[194:197], v[128:131], v[20:23]
	v_mfma_f32_16x16x32_bf16 v[12:15], v[198:201], v[128:131], v[12:15]
	s_waitcnt vmcnt(0) lgkmcnt(0)
	s_barrier
